# P0 expert-weight conversion stores marked nt (streamed, not re-read soon)
# speedup vs baseline: 1.0126x; 1.0009x over previous
; #define GAS __attribute__((address_space(1)))
; #define LAS __attribute__((address_space(3)))
; #define LDS_WAIT() asm volatile("s_waitcnt lgkmcnt(0)" ::: "memory")
; __device__ __forceinline__ unsigned pk4_fp8(float a, float b, float c, float d) { int r = __builtin_amdgcn_cvt_pk_fp8_f32(a, b, 0, false); r = __builtin_amdgcn_cvt_pk_fp8_f32(c, d, r, true); return (unsigned)r; }
; template <bool PAIR>
; __device__ __forceinline__ void p0_transpose_item8(const float* W, size_t ldw, int k0, int n0, unsigned char* WT, size_t drow0, int KdB, float scale, LAS unsigned* S, int lane) {
;     const int n4 = lane & 7, ks = lane >> 3;
;     const float* src = W + (size_t)(k0 + 4 * ks) * ldw + n0 + 4 * n4;
;     f32x4 a[4][4];
; #pragma unroll
;     for (int i = 0; i < 4; ++i)
; #pragma unroll
;         for (int r = 0; r < 4; ++r) a[i][r] = __builtin_nontemporal_load((const GAS f32x4*)(src + (size_t)(32 * i + r) * ldw));
; #pragma unroll
;     for (int i = 0; i < 4; ++i) { const int kq = ks + 8 * i;
; #pragma unroll
;         for (int j = 0; j < 4; ++j) { const int n = 4 * n4 + j; S[n * 32 + 4 * ((kq >> 2) ^ n4) + (kq & 3)] = pk4_fp8(a[i][0][j] * scale, a[i][1][j] * scale, a[i][2][j] * scale, a[i][3][j] * scale); } }
;     LDS_WAIT(); asm volatile("" ::: "memory");
.LBB0_61:
	s_lshl_b32 s27, s59, 1
	s_and_b32 s30, s27, 0x780
	s_addk_i32 s30, 0xfc00
	v_add_u32_e32 v56, s30, v3
	v_ashrrev_i32_e32 v57, 31, v56
	v_lshlrev_b64 v[56:57], 13, v[56:57]
	s_lshl_b32 s27, s59, 7
	v_lshl_add_u64 v[56:57], s[28:29], 0, v[56:57]
	s_and_b32 s28, s27, 0x1f80
	s_mov_b32 s29, s19
	v_lshl_add_u64 v[56:57], v[56:57], 0, s[28:29]
	v_lshlrev_b32_e32 v58, 2, v2
	v_mov_b32_e32 v59, v5
	v_lshl_add_u64 v[112:113], v[56:57], 0, v[58:59]
	v_add_co_u32_e32 v60, vcc, s39, v112
	s_lshl_b32 s31, s59, 5
	s_nop 0
	v_addc_co_u32_e32 v61, vcc, 0, v113, vcc
	v_add_co_u32_e32 v64, vcc, s40, v112
	global_load_dwordx4 v[56:59], v[112:113], off nt
	s_nop 0
	global_load_dwordx4 v[60:63], v[60:61], off nt
	v_addc_co_u32_e32 v65, vcc, 0, v113, vcc
	v_add_co_u32_e32 v68, vcc, s41, v112
	s_mov_b32 s27, s19
	s_nop 0
	v_addc_co_u32_e32 v69, vcc, 0, v113, vcc
	global_load_dwordx4 v[64:67], v[64:65], off nt
	s_nop 0
	global_load_dwordx4 v[68:71], v[68:69], off nt
	v_add_co_u32_e32 v72, vcc, s42, v112
	s_lshl_b64 s[28:29], s[26:27], 11
	s_nop 0
	v_addc_co_u32_e32 v73, vcc, 0, v113, vcc
	v_add_co_u32_e32 v76, vcc, s43, v112
	s_and_b32 s27, s31, 0x700
	s_nop 0
	v_addc_co_u32_e32 v77, vcc, 0, v113, vcc
	global_load_dwordx4 v[72:75], v[72:73], off nt
	s_nop 0
	global_load_dwordx4 v[76:79], v[76:77], off nt
	v_add_co_u32_e32 v80, vcc, s44, v112
	s_or_b32 s27, s28, s27
	s_nop 0
	v_addc_co_u32_e32 v81, vcc, 0, v113, vcc
	v_add_co_u32_e32 v84, vcc, s45, v112
	s_lshl_b32 s28, s59, 4
	s_nop 0
	v_addc_co_u32_e32 v85, vcc, 0, v113, vcc
	global_load_dwordx4 v[80:83], v[80:81], off nt
	s_nop 0
	global_load_dwordx4 v[84:87], v[84:85], off nt
	v_add_co_u32_e32 v88, vcc, s46, v112
	s_and_b32 s31, s28, 0x60
	s_nop 0
	v_addc_co_u32_e32 v89, vcc, 0, v113, vcc
	v_add_co_u32_e32 v92, vcc, s47, v112
	s_or_b32 s27, s27, s31
	s_nop 0
	v_addc_co_u32_e32 v93, vcc, 0, v113, vcc
	global_load_dwordx4 v[88:91], v[88:89], off nt
	s_nop 0
	global_load_dwordx4 v[92:95], v[92:93], off nt
	v_add_co_u32_e32 v96, vcc, s48, v112
	s_and_b32 s28, s28, 16
	s_nop 0
	v_addc_co_u32_e32 v97, vcc, 0, v113, vcc
	v_add_co_u32_e32 v100, vcc, s49, v112
	s_or_b32 s27, s27, s28
	s_nop 0
	v_addc_co_u32_e32 v101, vcc, 0, v113, vcc
	global_load_dwordx4 v[96:99], v[96:97], off nt
	s_nop 0
	global_load_dwordx4 v[100:103], v[100:101], off nt
	v_add_co_u32_e32 v104, vcc, s50, v112
	s_add_u32 s30, s92, s30
	s_nop 0
	v_addc_co_u32_e32 v105, vcc, 0, v113, vcc
	v_add_co_u32_e32 v108, vcc, s51, v112
	s_addc_u32 s31, s93, 0
	s_nop 0
	v_addc_co_u32_e32 v109, vcc, 0, v113, vcc
	global_load_dwordx4 v[104:107], v[104:105], off nt
	s_nop 0
	global_load_dwordx4 v[108:111], v[108:109], off nt
	v_add_co_u32_e32 v114, vcc, s52, v112
	s_waitcnt vmcnt(13)
	v_mul_f32_e32 v31, 0x42800000, v56
	v_addc_co_u32_e32 v115, vcc, 0, v113, vcc
	v_add_co_u32_e32 v116, vcc, s53, v112
	s_waitcnt vmcnt(12)
	v_mul_f32_e32 v55, 0x42800000, v60
	v_addc_co_u32_e32 v117, vcc, 0, v113, vcc
	global_load_dwordx4 v[112:115], v[114:115], off nt
	s_nop 0
	global_load_dwordx4 v[116:119], v[116:117], off nt
	s_waitcnt vmcnt(13)
	v_mul_f32_e32 v56, 0x42800000, v64
	v_mov_b32_e32 v64, v5
	v_cvt_pk_fp8_f32 v64, v31, v55
	v_mul_f32_e32 v31, 0x42800000, v57
	v_mul_f32_e32 v55, 0x42800000, v61
	v_mov_b32_e32 v57, v5
	v_cvt_pk_fp8_f32 v57, v31, v55
	s_waitcnt vmcnt(12)
	v_mul_f32_e32 v60, 0x42800000, v68
	v_mul_f32_e32 v31, 0x42800000, v65
	v_mul_f32_e32 v55, 0x42800000, v69
	v_cvt_pk_fp8_f32 v64, v56, v60 op_sel:[0,0,1]
	v_cvt_pk_fp8_f32 v57, v31, v55 op_sel:[0,0,1]
	v_mul_f32_e32 v55, 0x42800000, v58
	v_mul_f32_e32 v56, 0x42800000, v62
	v_mov_b32_e32 v60, v5
	v_cvt_pk_fp8_f32 v60, v55, v56
	v_mul_f32_e32 v55, 0x42800000, v59
	v_mul_f32_e32 v56, 0x42800000, v63
	v_mov_b32_e32 v59, v5
	v_cvt_pk_fp8_f32 v59, v55, v56
	v_add_u32_e32 v31, v15, v17
	ds_write2_b32 v31, v64, v57 offset1:32
	v_mul_f32_e32 v57, 0x42800000, v66
	v_mul_f32_e32 v58, 0x42800000, v70
	v_mul_f32_e32 v55, 0x42800000, v67
	v_mul_f32_e32 v56, 0x42800000, v71
	v_cvt_pk_fp8_f32 v60, v57, v58 op_sel:[0,0,1]
	v_cvt_pk_fp8_f32 v59, v55, v56 op_sel:[0,0,1]
	s_waitcnt vmcnt(11)
	v_mul_f32_e32 v55, 0x42800000, v72
	s_waitcnt vmcnt(10)
	v_mul_f32_e32 v56, 0x42800000, v76
	v_mov_b32_e32 v57, v5
	v_cvt_pk_fp8_f32 v57, v55, v56
	ds_write2_b32 v31, v60, v59 offset0:64 offset1:96
	s_waitcnt vmcnt(9)
	v_mul_f32_e32 v31, 0x42800000, v80
	s_waitcnt vmcnt(8)
; #define GAS __attribute__((address_space(1)))
; #define LAS __attribute__((address_space(3)))
; #define LDS_WAIT() asm volatile("s_waitcnt lgkmcnt(0)" ::: "memory")
; __device__ __forceinline__ unsigned pk4_fp8(float a, float b, float c, float d) { int r = __builtin_amdgcn_cvt_pk_fp8_f32(a, b, 0, false); r = __builtin_amdgcn_cvt_pk_fp8_f32(c, d, r, true); return (unsigned)r; }
; template <bool PAIR>
; __device__ __forceinline__ void p0_transpose_item8(const float* W, size_t ldw, int k0, int n0, unsigned char* WT, size_t drow0, int KdB, float scale, LAS unsigned* S, int lane) {
;     ...
;     for (int i = 0; i < 4; ++i) { const int kq = ks + 8 * i;
; #pragma unroll
;         for (int j = 0; j < 4; ++j) { const int n = 4 * n4 + j; S[n * 32 + 4 * ((kq >> 2) ^ n4) + (kq & 3)] = pk4_fp8(a[i][0][j] * scale, a[i][1][j] * scale, a[i][2][j] * scale, a[i][3][j] * scale); } }
;     LDS_WAIT(); asm volatile("" ::: "memory");
;     const int c = lane & 7;
; #pragma unroll
;     for (int j = 0; j < 4; ++j) { const int n = (lane >> 3) + 8 * j;
;         const v4u o = *(const LAS v4u*)(S + n * 32 + 4 * (c ^ ((n >> 2) & 7)));
;         const int dn = PAIR ? ((n & 7) + 8 * ((n >> 4) & 1) + 128 * ((n >> 3) & 1)) : n;
;         *(GAS v4u*)(WT + (drow0 + dn) * (size_t)KdB + k0 + 16 * c) = o; }
;     LDS_WAIT(); asm volatile("" ::: "memory");
	v_mul_f32_e32 v55, 0x42800000, v84
	v_cvt_pk_fp8_f32 v57, v31, v55 op_sel:[0,0,1]
	v_mul_f32_e32 v31, 0x42800000, v73
	v_mul_f32_e32 v55, 0x42800000, v77
	v_mov_b32_e32 v56, v5
	v_cvt_pk_fp8_f32 v56, v31, v55
	v_mul_f32_e32 v55, 0x42800000, v81
	v_mul_f32_e32 v58, 0x42800000, v85
	v_mov_b32_e32 v61, v5
	v_cvt_pk_fp8_f32 v56, v55, v58 op_sel:[0,0,1]
	v_mul_f32_e32 v55, 0x42800000, v74
	v_mul_f32_e32 v58, 0x42800000, v78
	v_cvt_pk_fp8_f32 v61, v55, v58
	v_mul_f32_e32 v55, 0x42800000, v75
	v_mul_f32_e32 v58, 0x42800000, v79
	v_mov_b32_e32 v62, v5
	v_cvt_pk_fp8_f32 v62, v55, v58
	v_mul_f32_e32 v55, 0x42800000, v83
	v_mul_f32_e32 v58, 0x42800000, v87
	v_mov_b32_e32 v63, v5
	v_cvt_pk_fp8_f32 v62, v55, v58 op_sel:[0,0,1]
	s_waitcnt vmcnt(7)
	v_mul_f32_e32 v55, 0x42800000, v88
	s_waitcnt vmcnt(6)
	v_mul_f32_e32 v58, 0x42800000, v92
	v_cvt_pk_fp8_f32 v63, v55, v58
	v_mul_f32_e32 v55, 0x42800000, v89
	v_mul_f32_e32 v58, 0x42800000, v93
	v_mov_b32_e32 v64, v5
	v_mul_f32_e32 v59, 0x42800000, v82
	v_mul_f32_e32 v60, 0x42800000, v86
	v_cvt_pk_fp8_f32 v64, v55, v58
	v_cvt_pk_fp8_f32 v61, v59, v60 op_sel:[0,0,1]
	v_add_u32_e32 v31, v19, v17
	s_waitcnt vmcnt(5)
	v_mul_f32_e32 v59, 0x42800000, v96
	s_waitcnt vmcnt(4)
	v_mul_f32_e32 v60, 0x42800000, v100
	v_mul_f32_e32 v55, 0x42800000, v97
	v_mul_f32_e32 v58, 0x42800000, v101
	v_cvt_pk_fp8_f32 v63, v59, v60 op_sel:[0,0,1]
	v_cvt_pk_fp8_f32 v64, v55, v58 op_sel:[0,0,1]
	ds_write2_b32 v31, v57, v56 offset1:32
	ds_write2_b32 v31, v61, v62 offset0:64 offset1:96
	v_mul_f32_e32 v55, 0x42800000, v90
	v_mul_f32_e32 v56, 0x42800000, v94
	v_mov_b32_e32 v59, v5
	v_cvt_pk_fp8_f32 v59, v55, v56
	v_mul_f32_e32 v55, 0x42800000, v91
	v_mul_f32_e32 v56, 0x42800000, v95
	v_mov_b32_e32 v60, v5
	v_cvt_pk_fp8_f32 v60, v55, v56
	v_mul_f32_e32 v55, 0x42800000, v99
	v_mul_f32_e32 v56, 0x42800000, v103
	v_mov_b32_e32 v61, v5
	v_cvt_pk_fp8_f32 v60, v55, v56 op_sel:[0,0,1]
	s_waitcnt vmcnt(3)
	v_mul_f32_e32 v55, 0x42800000, v104
	s_waitcnt vmcnt(2)
	v_mul_f32_e32 v56, 0x42800000, v108
	v_cvt_pk_fp8_f32 v61, v55, v56
	v_mul_f32_e32 v55, 0x42800000, v105
	v_mul_f32_e32 v56, 0x42800000, v109
	v_mov_b32_e32 v62, v5
	v_cvt_pk_fp8_f32 v62, v55, v56
	v_add_u32_e32 v31, v21, v17
	s_waitcnt vmcnt(1)
	v_mul_f32_e32 v55, 0x42800000, v113
	s_waitcnt vmcnt(0)
	v_mul_f32_e32 v56, 0x42800000, v117
	ds_write2_b32 v31, v63, v64 offset1:32
	v_cvt_pk_fp8_f32 v62, v55, v56 op_sel:[0,0,1]
	v_mul_f32_e32 v55, 0x42800000, v106
	v_mul_f32_e32 v56, 0x42800000, v110
	v_mov_b32_e32 v63, v5
	v_cvt_pk_fp8_f32 v63, v55, v56
	v_mul_f32_e32 v55, 0x42800000, v107
	v_mul_f32_e32 v56, 0x42800000, v111
	v_mov_b32_e32 v64, v5
	v_cvt_pk_fp8_f32 v64, v55, v56
	v_mul_f32_e32 v57, 0x42800000, v98
	v_mul_f32_e32 v58, 0x42800000, v102
	v_cvt_pk_fp8_f32 v59, v57, v58 op_sel:[0,0,1]
	v_mul_f32_e32 v57, 0x42800000, v112
	v_mul_f32_e32 v58, 0x42800000, v116
	v_cvt_pk_fp8_f32 v61, v57, v58 op_sel:[0,0,1]
	v_mul_f32_e32 v57, 0x42800000, v114
	v_mul_f32_e32 v58, 0x42800000, v118
	v_mul_f32_e32 v55, 0x42800000, v115
	v_mul_f32_e32 v56, 0x42800000, v119
	v_cvt_pk_fp8_f32 v63, v57, v58 op_sel:[0,0,1]
	v_cvt_pk_fp8_f32 v64, v55, v56 op_sel:[0,0,1]
	ds_write2_b32 v31, v59, v60 offset0:64 offset1:96
	v_add_u32_e32 v31, v33, v17
	ds_write2_b32 v31, v61, v62 offset1:32
	ds_write2_b32 v31, v63, v64 offset0:64 offset1:96
	s_waitcnt lgkmcnt(0)
	v_lshl_add_u64 v[56:57], s[30:31], 0, v[12:13]
	v_lshl_add_u64 v[64:65], v[56:57], 0, s[20:21]
	ds_read_b128 v[56:59], v34
	v_mov_b32_e32 v61, s29
	v_or_b32_e32 v60, s27, v14
	v_lshlrev_b64 v[60:61], 9, v[60:61]
	v_lshl_add_u64 v[66:67], v[64:65], 0, v[60:61]
	ds_read_b128 v[60:63], v36
	s_waitcnt lgkmcnt(1)
	global_store_dwordx4 v[66:67], v[56:59], off nt
	s_nop 1
	v_mov_b32_e32 v57, s29
	v_or_b32_e32 v56, s27, v16
	v_lshlrev_b64 v[56:57], 9, v[56:57]
	v_lshl_add_u64 v[56:57], v[64:65], 0, v[56:57]
	s_waitcnt lgkmcnt(0)
	global_store_dwordx4 v[56:57], v[60:63], off nt
	ds_read_b128 v[56:59], v37
	s_nop 0
	v_mov_b32_e32 v61, s29
	v_or_b32_e32 v60, s27, v18
	v_lshlrev_b64 v[60:61], 9, v[60:61]
	v_lshl_add_u64 v[66:67], v[64:65], 0, v[60:61]
	ds_read_b128 v[60:63], v38
	s_waitcnt lgkmcnt(1)
	global_store_dwordx4 v[66:67], v[56:59], off nt
	s_nop 1
	v_mov_b32_e32 v57, s29
	v_or_b32_e32 v56, s27, v20
	v_lshlrev_b64 v[56:57], 9, v[56:57]
	v_lshl_add_u64 v[56:57], v[64:65], 0, v[56:57]
	s_waitcnt lgkmcnt(0)
	global_store_dwordx4 v[56:57], v[60:63], off nt
	s_waitcnt lgkmcnt(0)
	s_mov_b64 s[28:29], 0

; #define GAS __attribute__((address_space(1)))
; #define LAS __attribute__((address_space(3)))
; #define LDS_WAIT() asm volatile("s_waitcnt lgkmcnt(0)" ::: "memory")
; __device__ __forceinline__ unsigned pk4_fp8(float a, float b, float c, float d) { int r = __builtin_amdgcn_cvt_pk_fp8_f32(a, b, 0, false); r = __builtin_amdgcn_cvt_pk_fp8_f32(c, d, r, true); return (unsigned)r; }
; template <bool PAIR>
; __device__ __forceinline__ void p0_transpose_item8(const float* W, size_t ldw, int k0, int n0, unsigned char* WT, size_t drow0, int KdB, float scale, LAS unsigned* S, int lane) {
;     const int n4 = lane & 7, ks = lane >> 3;
;     const float* src = W + (size_t)(k0 + 4 * ks) * ldw + n0 + 4 * n4;
;     f32x4 a[4][4];
; #pragma unroll
;     for (int i = 0; i < 4; ++i)
; #pragma unroll
;         for (int r = 0; r < 4; ++r) a[i][r] = __builtin_nontemporal_load((const GAS f32x4*)(src + (size_t)(32 * i + r) * ldw));
; #pragma unroll
;     for (int i = 0; i < 4; ++i) { const int kq = ks + 8 * i;
; #pragma unroll
;         for (int j = 0; j < 4; ++j) { const int n = 4 * n4 + j; S[n * 32 + 4 * ((kq >> 2) ^ n4) + (kq & 3)] = pk4_fp8(a[i][0][j] * scale, a[i][1][j] * scale, a[i][2][j] * scale, a[i][3][j] * scale); } }
;     LDS_WAIT(); asm volatile("" ::: "memory");
.LBB0_67:
	s_lshl_b32 s27, s59, 3
	s_and_b32 s30, s27, 0x780
	v_add_u32_e32 v56, s30, v3
	v_ashrrev_i32_e32 v57, 31, v56
	v_lshlrev_b64 v[56:57], 11, v[56:57]
	s_lshl_b32 s27, s59, 7
	v_lshl_add_u64 v[56:57], s[28:29], 0, v[56:57]
	s_and_b32 s28, s27, 0x780
	s_mov_b32 s29, s19
	v_lshl_add_u64 v[56:57], v[56:57], 0, s[28:29]
	v_lshlrev_b32_e32 v58, 2, v2
	v_mov_b32_e32 v59, v5
	v_lshl_add_u64 v[104:105], v[56:57], 0, v[58:59]
	global_load_dwordx4 v[56:59], v[104:105], off nt
	global_load_dwordx4 v[60:63], v[104:105], off offset:2048 nt
	v_add_co_u32_e32 v68, vcc, s64, v104
	v_mov_b32_e32 v31, v5
	s_nop 0
	v_addc_co_u32_e32 v69, vcc, 0, v105, vcc
	global_load_dwordx4 v[64:67], v[68:69], off nt
	s_nop 0
	global_load_dwordx4 v[68:71], v[68:69], off offset:2048 nt
	v_add_co_u32_e32 v76, vcc, s65, v104
	v_mov_b32_e32 v120, v5
	s_nop 0
	v_addc_co_u32_e32 v77, vcc, 0, v105, vcc
	v_add_co_u32_e32 v84, vcc, s66, v104
	v_mov_b32_e32 v121, v5
	s_nop 0
	v_addc_co_u32_e32 v85, vcc, 0, v105, vcc
	global_load_dwordx4 v[72:75], v[84:85], off offset:-4096 nt
	s_nop 0
	global_load_dwordx4 v[76:79], v[76:77], off offset:2048 nt
	s_nop 0
	global_load_dwordx4 v[80:83], v[84:85], off nt
	s_nop 0
	global_load_dwordx4 v[84:87], v[84:85], off offset:2048 nt
	v_add_co_u32_e32 v92, vcc, s67, v104
	v_mov_b32_e32 v122, v5
	s_nop 0
	v_addc_co_u32_e32 v93, vcc, 0, v105, vcc
	v_add_co_u32_e32 v100, vcc, s68, v104
	v_add_u32_e32 v55, v15, v17
	s_nop 0
	v_addc_co_u32_e32 v101, vcc, 0, v105, vcc
	global_load_dwordx4 v[88:91], v[100:101], off offset:-4096 nt
	s_nop 0
	global_load_dwordx4 v[92:95], v[92:93], off offset:2048 nt
	s_nop 0
	global_load_dwordx4 v[96:99], v[100:101], off nt
	s_nop 0
	global_load_dwordx4 v[100:103], v[100:101], off offset:2048 nt
	v_add_co_u32_e32 v108, vcc, s69, v104
	s_mov_b32 s27, s19
	s_nop 0
	v_addc_co_u32_e32 v109, vcc, 0, v105, vcc
	v_add_co_u32_e32 v116, vcc, s70, v104
	s_lshl_b32 s29, s59, 6
	s_nop 0
	v_addc_co_u32_e32 v117, vcc, 0, v105, vcc
	global_load_dwordx4 v[104:107], v[116:117], off offset:-4096 nt
	s_nop 0
	global_load_dwordx4 v[108:111], v[108:109], off offset:2048 nt
	s_nop 0
	global_load_dwordx4 v[112:115], v[116:117], off nt
	s_nop 0
	global_load_dwordx4 v[116:119], v[116:117], off offset:2048 nt
	s_lshr_b32 s31, s59, 1
	s_lshl_b64 s[26:27], s[26:27], 10
	s_and_b32 s29, s29, 0x300
	s_lshl_b32 s28, s59, 5
	s_and_b32 s31, s31, 0x80
	s_or_b32 s26, s26, s29
	s_and_b32 s28, s28, 0x60
	s_or_b32 s26, s26, s31
	s_or_b32 s26, s26, s28
	s_add_u32 s28, s92, s30
	s_addc_u32 s29, s93, 0
	s_waitcnt vmcnt(15)
	v_mul_f32_e32 v56, 0x42800000, v56
	s_waitcnt vmcnt(14)
	v_mul_f32_e32 v60, 0x42800000, v60
	v_mul_f32_e32 v57, 0x42800000, v57
	v_mul_f32_e32 v61, 0x42800000, v61
	v_cvt_pk_fp8_f32 v31, v56, v60
	v_cvt_pk_fp8_f32 v120, v57, v61
	v_mul_f32_e32 v58, 0x42800000, v58
	v_mul_f32_e32 v62, 0x42800000, v62
	v_mul_f32_e32 v59, 0x42800000, v59
	v_mul_f32_e32 v63, 0x42800000, v63
	s_waitcnt vmcnt(13)
	v_mul_f32_e32 v64, 0x42800000, v64
	s_waitcnt vmcnt(12)
	v_mul_f32_e32 v68, 0x42800000, v68
	v_mul_f32_e32 v56, 0x42800000, v65
	v_mul_f32_e32 v60, 0x42800000, v69
	v_cvt_pk_fp8_f32 v121, v58, v62
	v_cvt_pk_fp8_f32 v122, v59, v63
	v_cvt_pk_fp8_f32 v31, v64, v68 op_sel:[0,0,1]
	v_cvt_pk_fp8_f32 v120, v56, v60 op_sel:[0,0,1]
	v_mul_f32_e32 v57, 0x42800000, v66
	v_mul_f32_e32 v61, 0x42800000, v70
	v_mul_f32_e32 v58, 0x42800000, v67
	v_mul_f32_e32 v56, 0x42800000, v71
	v_cvt_pk_fp8_f32 v121, v57, v61 op_sel:[0,0,1]
	v_cvt_pk_fp8_f32 v122, v58, v56 op_sel:[0,0,1]
	ds_write2_b32 v55, v31, v120 offset1:32
	s_waitcnt vmcnt(11)
	v_mul_f32_e32 v31, 0x42800000, v72
	s_waitcnt vmcnt(10)
	v_mul_f32_e32 v56, 0x42800000, v76
	v_mov_b32_e32 v57, v5
	v_cvt_pk_fp8_f32 v57, v31, v56
	ds_write2_b32 v55, v121, v122 offset0:64 offset1:96
	s_waitcnt vmcnt(9)
	v_mul_f32_e32 v31, 0x42800000, v80
	s_waitcnt vmcnt(8)
; #define GAS __attribute__((address_space(1)))
; #define LAS __attribute__((address_space(3)))
; #define LDS_WAIT() asm volatile("s_waitcnt lgkmcnt(0)" ::: "memory")
; __device__ __forceinline__ unsigned pk4_fp8(float a, float b, float c, float d) { int r = __builtin_amdgcn_cvt_pk_fp8_f32(a, b, 0, false); r = __builtin_amdgcn_cvt_pk_fp8_f32(c, d, r, true); return (unsigned)r; }
; template <bool PAIR>
; __device__ __forceinline__ void p0_transpose_item8(const float* W, size_t ldw, int k0, int n0, unsigned char* WT, size_t drow0, int KdB, float scale, LAS unsigned* S, int lane) {
;     ...
;     for (int i = 0; i < 4; ++i) { const int kq = ks + 8 * i;
; #pragma unroll
;         for (int j = 0; j < 4; ++j) { const int n = 4 * n4 + j; S[n * 32 + 4 * ((kq >> 2) ^ n4) + (kq & 3)] = pk4_fp8(a[i][0][j] * scale, a[i][1][j] * scale, a[i][2][j] * scale, a[i][3][j] * scale); } }
;     LDS_WAIT(); asm volatile("" ::: "memory");
;     const int c = lane & 7;
; #pragma unroll
;     for (int j = 0; j < 4; ++j) { const int n = (lane >> 3) + 8 * j;
;         const v4u o = *(const LAS v4u*)(S + n * 32 + 4 * (c ^ ((n >> 2) & 7)));
;         const int dn = PAIR ? ((n & 7) + 8 * ((n >> 4) & 1) + 128 * ((n >> 3) & 1)) : n;
;         *(GAS v4u*)(WT + (drow0 + dn) * (size_t)KdB + k0 + 16 * c) = o; }
;     LDS_WAIT(); asm volatile("" ::: "memory");
	v_mul_f32_e32 v55, 0x42800000, v84
	v_cvt_pk_fp8_f32 v57, v31, v55 op_sel:[0,0,1]
	v_mul_f32_e32 v31, 0x42800000, v73
	v_mul_f32_e32 v55, 0x42800000, v77
	v_mov_b32_e32 v56, v5
	v_cvt_pk_fp8_f32 v56, v31, v55
	v_mul_f32_e32 v55, 0x42800000, v81
	v_mul_f32_e32 v58, 0x42800000, v85
	v_mov_b32_e32 v61, v5
	v_cvt_pk_fp8_f32 v56, v55, v58 op_sel:[0,0,1]
	v_mul_f32_e32 v55, 0x42800000, v74
	v_mul_f32_e32 v58, 0x42800000, v78
	v_cvt_pk_fp8_f32 v61, v55, v58
	v_mul_f32_e32 v55, 0x42800000, v75
	v_mul_f32_e32 v58, 0x42800000, v79
	v_mov_b32_e32 v62, v5
	v_cvt_pk_fp8_f32 v62, v55, v58
	v_mul_f32_e32 v55, 0x42800000, v83
	v_mul_f32_e32 v58, 0x42800000, v87
	v_mov_b32_e32 v63, v5
	v_cvt_pk_fp8_f32 v62, v55, v58 op_sel:[0,0,1]
	s_waitcnt vmcnt(7)
	v_mul_f32_e32 v55, 0x42800000, v88
	s_waitcnt vmcnt(6)
	v_mul_f32_e32 v58, 0x42800000, v92
	v_cvt_pk_fp8_f32 v63, v55, v58
	v_mul_f32_e32 v55, 0x42800000, v89
	v_mul_f32_e32 v58, 0x42800000, v93
	v_mov_b32_e32 v64, v5
	v_mul_f32_e32 v59, 0x42800000, v82
	v_mul_f32_e32 v60, 0x42800000, v86
	v_cvt_pk_fp8_f32 v64, v55, v58
	v_cvt_pk_fp8_f32 v61, v59, v60 op_sel:[0,0,1]
	v_add_u32_e32 v31, v19, v17
	s_waitcnt vmcnt(5)
	v_mul_f32_e32 v59, 0x42800000, v96
	s_waitcnt vmcnt(4)
	v_mul_f32_e32 v60, 0x42800000, v100
	v_mul_f32_e32 v55, 0x42800000, v97
	v_mul_f32_e32 v58, 0x42800000, v101
	v_cvt_pk_fp8_f32 v63, v59, v60 op_sel:[0,0,1]
	v_cvt_pk_fp8_f32 v64, v55, v58 op_sel:[0,0,1]
	ds_write2_b32 v31, v57, v56 offset1:32
	ds_write2_b32 v31, v61, v62 offset0:64 offset1:96
	v_mul_f32_e32 v55, 0x42800000, v90
	v_mul_f32_e32 v56, 0x42800000, v94
	v_mov_b32_e32 v59, v5
	v_cvt_pk_fp8_f32 v59, v55, v56
	v_mul_f32_e32 v55, 0x42800000, v91
	v_mul_f32_e32 v56, 0x42800000, v95
	v_mov_b32_e32 v60, v5
	v_cvt_pk_fp8_f32 v60, v55, v56
	v_mul_f32_e32 v55, 0x42800000, v99
	v_mul_f32_e32 v56, 0x42800000, v103
	v_mov_b32_e32 v61, v5
	v_cvt_pk_fp8_f32 v60, v55, v56 op_sel:[0,0,1]
	s_waitcnt vmcnt(3)
	v_mul_f32_e32 v55, 0x42800000, v104
	s_waitcnt vmcnt(2)
	v_mul_f32_e32 v56, 0x42800000, v108
	v_cvt_pk_fp8_f32 v61, v55, v56
	v_mul_f32_e32 v55, 0x42800000, v105
	v_mul_f32_e32 v56, 0x42800000, v109
	v_mov_b32_e32 v62, v5
	v_cvt_pk_fp8_f32 v62, v55, v56
	v_add_u32_e32 v31, v21, v17
	s_waitcnt vmcnt(1)
	v_mul_f32_e32 v55, 0x42800000, v113
	s_waitcnt vmcnt(0)
	v_mul_f32_e32 v56, 0x42800000, v117
	ds_write2_b32 v31, v63, v64 offset1:32
	v_cvt_pk_fp8_f32 v62, v55, v56 op_sel:[0,0,1]
	v_mul_f32_e32 v55, 0x42800000, v106
	v_mul_f32_e32 v56, 0x42800000, v110
	v_mov_b32_e32 v63, v5
	v_cvt_pk_fp8_f32 v63, v55, v56
	v_mul_f32_e32 v55, 0x42800000, v107
	v_mul_f32_e32 v56, 0x42800000, v111
	v_mov_b32_e32 v64, v5
	v_cvt_pk_fp8_f32 v64, v55, v56
	v_mul_f32_e32 v57, 0x42800000, v98
	v_mul_f32_e32 v58, 0x42800000, v102
	v_cvt_pk_fp8_f32 v59, v57, v58 op_sel:[0,0,1]
	v_mul_f32_e32 v57, 0x42800000, v112
	v_mul_f32_e32 v58, 0x42800000, v116
	v_cvt_pk_fp8_f32 v61, v57, v58 op_sel:[0,0,1]
	v_mul_f32_e32 v57, 0x42800000, v114
	v_mul_f32_e32 v58, 0x42800000, v118
	v_mul_f32_e32 v55, 0x42800000, v115
	v_mul_f32_e32 v56, 0x42800000, v119
	v_cvt_pk_fp8_f32 v63, v57, v58 op_sel:[0,0,1]
	v_cvt_pk_fp8_f32 v64, v55, v56 op_sel:[0,0,1]
	ds_write2_b32 v31, v59, v60 offset0:64 offset1:96
	v_add_u32_e32 v31, v33, v17
	ds_write2_b32 v31, v61, v62 offset1:32
	ds_write2_b32 v31, v63, v64 offset0:64 offset1:96
	s_waitcnt lgkmcnt(0)
	v_lshl_add_u64 v[56:57], s[28:29], 0, v[12:13]
	v_lshl_add_u64 v[64:65], v[56:57], 0, s[22:23]
	ds_read_b128 v[56:59], v34
	v_lshl_add_u64 v[60:61], s[26:27], 0, v[0:1]
	v_lshlrev_b64 v[60:61], 11, v[60:61]
	v_lshl_add_u64 v[66:67], v[64:65], 0, v[60:61]
	ds_read_b128 v[60:63], v36
	s_waitcnt lgkmcnt(1)
	global_store_dwordx4 v[66:67], v[56:59], off nt
	s_nop 1
	v_lshl_add_u64 v[56:57], s[26:27], 0, v[6:7]
	v_lshlrev_b64 v[56:57], 11, v[56:57]
	v_lshl_add_u64 v[56:57], v[64:65], 0, v[56:57]
	s_waitcnt lgkmcnt(0)
	global_store_dwordx4 v[56:57], v[60:63], off nt
	ds_read_b128 v[56:59], v37
	s_nop 0
	v_lshl_add_u64 v[60:61], s[26:27], 0, v[8:9]
	v_lshlrev_b64 v[60:61], 11, v[60:61]
	v_lshl_add_u64 v[66:67], v[64:65], 0, v[60:61]
	ds_read_b128 v[60:63], v38
	s_waitcnt lgkmcnt(1)
	global_store_dwordx4 v[66:67], v[56:59], off nt
	s_nop 1
	v_lshl_add_u64 v[56:57], s[26:27], 0, v[10:11]
	v_lshlrev_b64 v[56:57], 11, v[56:57]
	v_lshl_add_u64 v[56:57], v[64:65], 0, v[56:57]
	s_waitcnt lgkmcnt(0)
	global_store_dwordx4 v[56:57], v[60:63], off nt
	s_waitcnt lgkmcnt(0)
	s_mov_b64 s[26:27], 0
